# v7 plus P0 weight-copy stores (bf16 / fp8 in-projection and projection weights) with default cache policy instead of nt
# baseline (speedup 1.0000x reference)
.LBB0_38:
	ds_read_b128 v[112:115], v102
	ds_read_b128 v[116:119], v103
	v_lshl_add_u64 v[120:121], s[10:11], 0, v[72:73]
	v_mov_b32_e32 v75, v73
	v_lshl_add_u64 v[122:123], v[120:121], 0, v[74:75]
	v_mov_b32_e32 v77, v73
	s_waitcnt lgkmcnt(1)
	global_store_dwordx4 v[122:123], v[112:115], off
	v_lshl_add_u64 v[122:123], v[120:121], 0, v[76:77]
	ds_read_b128 v[112:115], v104
	s_waitcnt lgkmcnt(1)
	global_store_dwordx4 v[122:123], v[116:119], off
	ds_read_b128 v[116:119], v105
	v_mov_b32_e32 v79, v73
	v_lshl_add_u64 v[122:123], v[120:121], 0, v[78:79]
	v_mov_b32_e32 v81, v73
	s_waitcnt lgkmcnt(1)
	global_store_dwordx4 v[122:123], v[112:115], off
	v_lshl_add_u64 v[122:123], v[120:121], 0, v[80:81]
	ds_read_b128 v[112:115], v106
	s_waitcnt lgkmcnt(1)
	global_store_dwordx4 v[122:123], v[116:119], off
	ds_read_b128 v[116:119], v107
	v_mov_b32_e32 v83, v73
	v_lshl_add_u64 v[122:123], v[120:121], 0, v[82:83]
	v_mov_b32_e32 v85, v73
	s_waitcnt lgkmcnt(1)
	global_store_dwordx4 v[122:123], v[112:115], off
	v_lshl_add_u64 v[122:123], v[120:121], 0, v[84:85]
	ds_read_b128 v[112:115], v108
	s_waitcnt lgkmcnt(1)
	global_store_dwordx4 v[122:123], v[116:119], off
	ds_read_b128 v[116:119], v109
	v_mov_b32_e32 v87, v73
	v_lshl_add_u64 v[122:123], v[120:121], 0, v[86:87]
	v_mov_b32_e32 v89, v73
	s_waitcnt lgkmcnt(1)
	global_store_dwordx4 v[122:123], v[112:115], off
	s_add_i32 s85, s85, s86
	s_andn2_b64 vcc, exec, s[14:15]
	v_lshl_add_u64 v[112:113], v[120:121], 0, v[88:89]
	s_mov_b64 s[10:11], s[12:13]
	s_waitcnt lgkmcnt(0)
	global_store_dwordx4 v[112:113], v[116:119], off
	s_barrier
	s_cbranch_vccz .LBB0_44

.LBB0_50:
	ds_read_b128 v[88:91], v82
	v_lshl_add_u64 v[100:101], s[14:15], 0, v[70:71]
	ds_read_b128 v[92:95], v83
	ds_read_b128 v[96:99], v84
	v_lshl_add_u64 v[102:103], v[100:101], 0, v[72:73]
	s_add_i32 s31, s31, s34
	s_waitcnt lgkmcnt(2)
	global_store_dwordx4 v[102:103], v[88:91], off
	ds_read_b128 v[88:91], v85
	v_lshl_add_u64 v[102:103], v[100:101], 0, v[74:75]
	s_waitcnt lgkmcnt(2)
	global_store_dwordx4 v[102:103], v[92:95], off
	s_andn2_b64 vcc, exec, s[38:39]
	s_mov_b64 s[14:15], s[16:17]
	v_lshl_add_u64 v[92:93], v[100:101], 0, v[76:77]
	s_waitcnt lgkmcnt(1)
	global_store_dwordx4 v[92:93], v[96:99], off
	v_lshl_add_u64 v[92:93], v[100:101], 0, v[78:79]
	s_waitcnt lgkmcnt(0)
	global_store_dwordx4 v[92:93], v[88:91], off
	s_barrier
	s_cbranch_vccz .LBB0_60
